# passCU: BN1 constants for next tile prefetched from LDS at loop bottom; node-id clamp only near the end of the edge list
# speedup vs baseline: 1.0857x; 1.0030x over previous
.LBB8_4:
	s_load_dwordx2 s[12:13], s[0:1], 0xa8
	s_load_dwordx2 s[18:19], s[0:1], 0x98
	s_waitcnt lgkmcnt(0)
	s_sub_i32 s4, s28, s20
	s_add_i32 s4, s4, 31
	v_and_b32_e32 v1, 63, v0
	s_ashr_i32 s15, s4, 5
	s_cmp_lt_i32 s15, 1
	v_or_b32_e32 v90, s14, v98
	v_and_b32_e32 v100, 32, v0
	v_lshlrev_b32_e32 v99, 4, v1
	s_cbranch_scc1 .LBB8_7
	s_load_dwordx8 s[4:11], s[0:1], 0x0
	s_load_dwordx2 s[24:25], s[0:1], 0x20
	s_load_dwordx2 s[30:31], s[0:1], 0x80
	v_and_b32_e32 v34, 7, v1
	v_lshlrev_b32_e32 v34, 4, v34
	v_lshrrev_b32_e32 v35, 3, v1
	s_lshl_b32 s32, s3, 12
	s_add_i32 s33, s32, 0x2000
	s_add_i32 s32, s32, 0xb500
	s_cmp_lt_u32 s3, 2
	s_cselect_b32 s32, s33, s32
	v_lshlrev_b32_e32 v36, 1, v35
	v_and_b32_e32 v36, 7, v36
	v_or_b32_e32 v37, 1, v36
	v_lshlrev_b32_e32 v36, 4, v36
	v_lshlrev_b32_e32 v37, 4, v37
	v_xor_b32_e32 v36, v36, v34
	v_xor_b32_e32 v37, v37, v34
	v_lshl_add_u32 v39, v35, 9, s32
	v_add_u32_e32 v36, v36, v39
	v_add_u32_e32 v37, v37, v39
	v_lshrrev_b32_e32 v38, 1, v98
	v_and_b32_e32 v38, 7, v38
	v_lshrrev_b32_e32 v39, 3, v100
	v_xor_b32_e32 v38, v38, v39
	v_lshlrev_b32_e32 v38, 4, v38
	v_lshl_add_u32 v39, v98, 7, s32
	v_add_u32_e32 v38, v38, v39
	v_lshlrev_b32_e32 v35, 4, v35
	s_mov_b32 s35, 0x1869f
	v_mov_b32_e32 v2, 0
	v_mov_b32_e32 v3, 0
	v_mov_b32_e32 v4, 0
	v_mov_b32_e32 v5, 0
	v_mov_b32_e32 v6, 0
	v_mov_b32_e32 v7, 0
	v_mov_b32_e32 v8, 0
	v_mov_b32_e32 v9, 0
	v_mov_b32_e32 v10, 0
	v_mov_b32_e32 v11, 0
	v_mov_b32_e32 v12, 0
	v_mov_b32_e32 v13, 0
	v_mov_b32_e32 v14, 0
	v_mov_b32_e32 v15, 0
	v_mov_b32_e32 v16, 0
	v_mov_b32_e32 v17, 0
	v_mov_b32_e32 v18, 0
	v_mov_b32_e32 v19, 0
	v_mov_b32_e32 v20, 0
	v_mov_b32_e32 v21, 0
	v_mov_b32_e32 v22, 0
	v_mov_b32_e32 v23, 0
	v_mov_b32_e32 v24, 0
	v_mov_b32_e32 v25, 0
	v_mov_b32_e32 v26, 0
	v_mov_b32_e32 v27, 0
	v_mov_b32_e32 v28, 0
	v_mov_b32_e32 v29, 0
	v_mov_b32_e32 v30, 0
	v_mov_b32_e32 v31, 0
	v_mov_b32_e32 v32, 0
	v_mov_b32_e32 v33, 0
	s_waitcnt vmcnt(0) lgkmcnt(0)
	v_mov_b32_e32 v42, v70
	v_mov_b32_e32 v43, v71
	v_mov_b32_e32 v44, v72
	v_mov_b32_e32 v45, v73
	v_mov_b32_e32 v46, v74
	v_mov_b32_e32 v47, v75
	v_mov_b32_e32 v48, v76
	v_mov_b32_e32 v49, v77
	v_mov_b32_e32 v50, v78
	v_mov_b32_e32 v51, v79
	v_mov_b32_e32 v52, v80
	v_mov_b32_e32 v53, v81
	v_lshlrev_b32_e32 v39, 2, v90
	global_load_dword v40, v39, s[30:31]
	global_load_dword v41, v39, s[30:31] offset:4
	s_lshl_b32 s34, s20, 2
	v_min_u32_e32 v42, s35, v42
	v_min_u32_e32 v46, s35, v46
	v_min_u32_e32 v43, s35, v43
	v_min_u32_e32 v47, s35, v47
	v_min_u32_e32 v44, s35, v44
	v_min_u32_e32 v48, s35, v48
	v_min_u32_e32 v45, s35, v45
	v_min_u32_e32 v49, s35, v49
	v_lshl_or_b32 v42, v42, 7, v34
	v_lshl_or_b32 v46, v46, 7, v34
	v_lshl_or_b32 v43, v43, 7, v34
	v_lshl_or_b32 v47, v47, 7, v34
	v_lshl_or_b32 v44, v44, 7, v34
	v_lshl_or_b32 v48, v48, 7, v34
	v_lshl_or_b32 v45, v45, 7, v34
	v_lshl_or_b32 v49, v49, 7, v34
	global_load_dwordx4 v[70:73], v42, s[24:25]
	global_load_dwordx4 v[74:77], v43, s[24:25]
	global_load_dwordx4 v[78:81], v44, s[24:25]
	global_load_dwordx4 v[82:85], v45, s[24:25]
	global_load_dwordx4 v[86:89], v46, s[10:11]
	global_load_dwordx4 v[90:93], v47, s[10:11]
	global_load_dwordx4 v[94:97], v48, s[10:11]
	global_load_dwordx4 v[102:105], v49, s[10:11]
	s_add_i32 s34, s34, 0x80
	v_add_u32_e32 v39, s34, v35
	global_load_dwordx4 v[42:45], v39, s[4:5]
	global_load_dwordx4 v[46:49], v39, s[6:7]
	v_lshlrev_b32_e32 v39, 1, v34
	ds_read_b128 v[112:115], v39 offset:53248
	ds_read_b128 v[116:119], v39 offset:53760
	ds_read_b128 v[120:123], v39 offset:53504

.Lcu_noclampe:
	v_lshlrev_b32_e32 v39, 1, v34
	s_waitcnt lgkmcnt(0)
	v_lshlrev_b32_e32 v124, 16, v86
	v_and_b32_e32 v125, 0xffff0000, v86
	v_lshlrev_b32_e32 v126, 16, v70
	v_and_b32_e32 v127, 0xffff0000, v70
	v_add_f32_e32 v124, v126, v124
	v_add_f32_e32 v125, v127, v125
	v_fma_f32 v126, v116, v50, v120
	v_fma_f32 v127, v117, v50, v121
	v_fmac_f32_e32 v126, v112, v124
	v_fmac_f32_e32 v127, v113, v125
	v_max_f32_e32 v126, 0, v126
	v_max_f32_e32 v127, 0, v127
	v_cvt_pk_f16_f32 v54, v126, v127
	v_lshlrev_b32_e32 v106, 16, v87
	v_and_b32_e32 v107, 0xffff0000, v87
	v_lshlrev_b32_e32 v108, 16, v71
	v_and_b32_e32 v109, 0xffff0000, v71
	v_add_f32_e32 v106, v108, v106
	v_add_f32_e32 v107, v109, v107
	v_fma_f32 v108, v118, v50, v122
	v_fma_f32 v109, v119, v50, v123
	v_fmac_f32_e32 v108, v114, v106
	v_fmac_f32_e32 v109, v115, v107
	v_max_f32_e32 v108, 0, v108
	v_max_f32_e32 v109, 0, v109
	v_cvt_pk_f16_f32 v55, v108, v109
	ds_write_b64 v36, v[54:55] offset:0
	v_lshlrev_b32_e32 v124, 16, v90
	v_and_b32_e32 v125, 0xffff0000, v90
	v_lshlrev_b32_e32 v126, 16, v74
	v_and_b32_e32 v127, 0xffff0000, v74
	v_add_f32_e32 v124, v126, v124
	v_add_f32_e32 v125, v127, v125
	v_fma_f32 v126, v116, v51, v120
	v_fma_f32 v127, v117, v51, v121
	v_fmac_f32_e32 v126, v112, v124
	v_fmac_f32_e32 v127, v113, v125
	v_max_f32_e32 v126, 0, v126
	v_max_f32_e32 v127, 0, v127
	v_cvt_pk_f16_f32 v56, v126, v127
	v_lshlrev_b32_e32 v106, 16, v91
	v_and_b32_e32 v107, 0xffff0000, v91
	v_lshlrev_b32_e32 v108, 16, v75
	v_and_b32_e32 v109, 0xffff0000, v75
	v_add_f32_e32 v106, v108, v106
	v_add_f32_e32 v107, v109, v107
	v_fma_f32 v108, v118, v51, v122
	v_fma_f32 v109, v119, v51, v123
	v_fmac_f32_e32 v108, v114, v106
	v_fmac_f32_e32 v109, v115, v107
	v_max_f32_e32 v108, 0, v108
	v_max_f32_e32 v109, 0, v109
	v_cvt_pk_f16_f32 v57, v108, v109
	ds_write_b64 v36, v[56:57] offset:128
	v_lshlrev_b32_e32 v124, 16, v94
	v_and_b32_e32 v125, 0xffff0000, v94
	v_lshlrev_b32_e32 v126, 16, v78
	v_and_b32_e32 v127, 0xffff0000, v78
	v_add_f32_e32 v124, v126, v124
	v_add_f32_e32 v125, v127, v125
	v_fma_f32 v126, v116, v52, v120
	v_fma_f32 v127, v117, v52, v121
	v_fmac_f32_e32 v126, v112, v124
	v_fmac_f32_e32 v127, v113, v125
	v_max_f32_e32 v126, 0, v126
	v_max_f32_e32 v127, 0, v127
	v_cvt_pk_f16_f32 v54, v126, v127
	v_lshlrev_b32_e32 v106, 16, v95
	v_and_b32_e32 v107, 0xffff0000, v95
	v_lshlrev_b32_e32 v108, 16, v79
	v_and_b32_e32 v109, 0xffff0000, v79
	v_add_f32_e32 v106, v108, v106
	v_add_f32_e32 v107, v109, v107
	v_fma_f32 v108, v118, v52, v122
	v_fma_f32 v109, v119, v52, v123
	v_fmac_f32_e32 v108, v114, v106
	v_fmac_f32_e32 v109, v115, v107
	v_max_f32_e32 v108, 0, v108
	v_max_f32_e32 v109, 0, v109
	v_cvt_pk_f16_f32 v55, v108, v109
	ds_write_b64 v37, v[54:55] offset:256
	v_lshlrev_b32_e32 v124, 16, v102
	v_and_b32_e32 v125, 0xffff0000, v102
	v_lshlrev_b32_e32 v126, 16, v82
	v_and_b32_e32 v127, 0xffff0000, v82
	v_add_f32_e32 v124, v126, v124
	v_add_f32_e32 v125, v127, v125
	v_fma_f32 v126, v116, v53, v120
	v_fma_f32 v127, v117, v53, v121
	v_fmac_f32_e32 v126, v112, v124
	v_fmac_f32_e32 v127, v113, v125
	v_max_f32_e32 v126, 0, v126
	v_max_f32_e32 v127, 0, v127
	v_cvt_pk_f16_f32 v56, v126, v127
	v_lshlrev_b32_e32 v106, 16, v103
	v_and_b32_e32 v107, 0xffff0000, v103
	v_lshlrev_b32_e32 v108, 16, v83
	v_and_b32_e32 v109, 0xffff0000, v83
	v_add_f32_e32 v106, v108, v106
	v_add_f32_e32 v107, v109, v107
	v_fma_f32 v108, v118, v53, v122
	v_fma_f32 v109, v119, v53, v123
	v_fmac_f32_e32 v108, v114, v106
	v_fmac_f32_e32 v109, v115, v107
	v_max_f32_e32 v108, 0, v108
	v_max_f32_e32 v109, 0, v109
	v_cvt_pk_f16_f32 v57, v108, v109
	ds_write_b64 v37, v[56:57] offset:384
	ds_read_b128 v[112:115], v39 offset:53264
	ds_read_b128 v[116:119], v39 offset:53776
	ds_read_b128 v[120:123], v39 offset:53520
	s_waitcnt lgkmcnt(0)
	v_lshlrev_b32_e32 v124, 16, v88
	v_and_b32_e32 v125, 0xffff0000, v88
	v_lshlrev_b32_e32 v126, 16, v72
	v_and_b32_e32 v127, 0xffff0000, v72
	v_add_f32_e32 v124, v126, v124
	v_add_f32_e32 v125, v127, v125
	v_fma_f32 v126, v116, v50, v120
	v_fma_f32 v127, v117, v50, v121
	v_fmac_f32_e32 v126, v112, v124
	v_fmac_f32_e32 v127, v113, v125
	v_max_f32_e32 v126, 0, v126
	v_max_f32_e32 v127, 0, v127
	v_cvt_pk_f16_f32 v54, v126, v127
	v_lshlrev_b32_e32 v106, 16, v89
	v_and_b32_e32 v107, 0xffff0000, v89
	v_lshlrev_b32_e32 v108, 16, v73
	v_and_b32_e32 v109, 0xffff0000, v73
	v_add_f32_e32 v106, v108, v106
	v_add_f32_e32 v107, v109, v107
	v_fma_f32 v108, v118, v50, v122
	v_fma_f32 v109, v119, v50, v123
	v_fmac_f32_e32 v108, v114, v106
	v_fmac_f32_e32 v109, v115, v107
	v_max_f32_e32 v108, 0, v108
	v_max_f32_e32 v109, 0, v109
	v_cvt_pk_f16_f32 v55, v108, v109
	ds_write_b64 v36, v[54:55] offset:8
	v_lshlrev_b32_e32 v124, 16, v92
	v_and_b32_e32 v125, 0xffff0000, v92
	v_lshlrev_b32_e32 v126, 16, v76
	v_and_b32_e32 v127, 0xffff0000, v76
	v_add_f32_e32 v124, v126, v124
	v_add_f32_e32 v125, v127, v125
	v_fma_f32 v126, v116, v51, v120
	v_fma_f32 v127, v117, v51, v121
	v_fmac_f32_e32 v126, v112, v124
	v_fmac_f32_e32 v127, v113, v125
	v_max_f32_e32 v126, 0, v126
	v_max_f32_e32 v127, 0, v127
	v_cvt_pk_f16_f32 v56, v126, v127
	v_lshlrev_b32_e32 v106, 16, v93
	v_and_b32_e32 v107, 0xffff0000, v93
	v_lshlrev_b32_e32 v108, 16, v77
	v_and_b32_e32 v109, 0xffff0000, v77
	v_add_f32_e32 v106, v108, v106
	v_add_f32_e32 v107, v109, v107
	v_fma_f32 v108, v118, v51, v122
	v_fma_f32 v109, v119, v51, v123
	v_fmac_f32_e32 v108, v114, v106
	v_fmac_f32_e32 v109, v115, v107
	v_max_f32_e32 v108, 0, v108
	v_max_f32_e32 v109, 0, v109
	v_cvt_pk_f16_f32 v57, v108, v109
	ds_write_b64 v36, v[56:57] offset:136
	v_lshlrev_b32_e32 v124, 16, v96
	v_and_b32_e32 v125, 0xffff0000, v96
	v_lshlrev_b32_e32 v126, 16, v80
	v_and_b32_e32 v127, 0xffff0000, v80
	v_add_f32_e32 v124, v126, v124
	v_add_f32_e32 v125, v127, v125
	v_fma_f32 v126, v116, v52, v120
	v_fma_f32 v127, v117, v52, v121
	v_fmac_f32_e32 v126, v112, v124
	v_fmac_f32_e32 v127, v113, v125
	v_max_f32_e32 v126, 0, v126
	v_max_f32_e32 v127, 0, v127
	v_cvt_pk_f16_f32 v54, v126, v127
	v_lshlrev_b32_e32 v106, 16, v97
	v_and_b32_e32 v107, 0xffff0000, v97
	v_lshlrev_b32_e32 v108, 16, v81
	v_and_b32_e32 v109, 0xffff0000, v81
	v_add_f32_e32 v106, v108, v106
	v_add_f32_e32 v107, v109, v107
	v_fma_f32 v108, v118, v52, v122
	v_fma_f32 v109, v119, v52, v123
	v_fmac_f32_e32 v108, v114, v106
	v_fmac_f32_e32 v109, v115, v107
	v_max_f32_e32 v108, 0, v108
	v_max_f32_e32 v109, 0, v109
	v_cvt_pk_f16_f32 v55, v108, v109
	ds_write_b64 v37, v[54:55] offset:264
	v_lshlrev_b32_e32 v124, 16, v104
	v_and_b32_e32 v125, 0xffff0000, v104
	v_lshlrev_b32_e32 v126, 16, v84
	v_and_b32_e32 v127, 0xffff0000, v84
	v_add_f32_e32 v124, v126, v124
	v_add_f32_e32 v125, v127, v125
	v_fma_f32 v126, v116, v53, v120
	v_fma_f32 v127, v117, v53, v121
	v_fmac_f32_e32 v126, v112, v124
	v_fmac_f32_e32 v127, v113, v125
	v_max_f32_e32 v126, 0, v126
	v_max_f32_e32 v127, 0, v127
	v_cvt_pk_f16_f32 v56, v126, v127
	v_lshlrev_b32_e32 v106, 16, v105
	v_and_b32_e32 v107, 0xffff0000, v105
	v_lshlrev_b32_e32 v108, 16, v85
	v_and_b32_e32 v109, 0xffff0000, v85
	v_add_f32_e32 v106, v108, v106
	v_add_f32_e32 v107, v109, v107
	v_fma_f32 v108, v118, v53, v122
	v_fma_f32 v109, v119, v53, v123
	v_fmac_f32_e32 v108, v114, v106
	v_fmac_f32_e32 v109, v115, v107
	v_max_f32_e32 v108, 0, v108
	v_max_f32_e32 v109, 0, v109
	v_cvt_pk_f16_f32 v57, v108, v109
	ds_write_b64 v37, v[56:57] offset:392
	s_waitcnt vmcnt(0)
	s_cmp_eq_u32 s15, 1
	s_cbranch_scc1 .Lcu_skip1
	s_add_i32 s36, s20, 0x60
	s_cmp_le_u32 s36, 0xf4240
	s_cbranch_scc1 .Lcu_noclampsd
	v_min_u32_e32 v42, s35, v42
	v_min_u32_e32 v46, s35, v46
	v_min_u32_e32 v43, s35, v43
	v_min_u32_e32 v47, s35, v47
	v_min_u32_e32 v44, s35, v44
	v_min_u32_e32 v48, s35, v48
	v_min_u32_e32 v45, s35, v45
	v_min_u32_e32 v49, s35, v49
.Lcu_noclampsd:
	v_lshl_or_b32 v42, v42, 7, v34
	v_lshl_or_b32 v46, v46, 7, v34
	v_lshl_or_b32 v43, v43, 7, v34
	v_lshl_or_b32 v47, v47, 7, v34
	v_lshl_or_b32 v44, v44, 7, v34
	v_lshl_or_b32 v48, v48, 7, v34
	v_lshl_or_b32 v45, v45, 7, v34
	v_lshl_or_b32 v49, v49, 7, v34
	global_load_dwordx4 v[70:73], v42, s[24:25]
	global_load_dwordx4 v[74:77], v43, s[24:25]
	global_load_dwordx4 v[78:81], v44, s[24:25]
	global_load_dwordx4 v[82:85], v45, s[24:25]
	s_lshl_b32 s34, s20, 2
	s_add_i32 s34, s34, 0x80
	v_add_u32_e32 v39, s34, v35
	global_load_dwordx4 v[50:53], v39, s[8:9]

.Lcu_skip2:
	s_nop 9
	v_fma_f32 v110, v67, v112, v69
	v_fma_f32 v111, v67, v113, v69
	v_max_f32_e32 v110, 0, v110
	v_max_f32_e32 v111, 0, v111
	v_cvt_pk_bf16_f32 v106, v110, v111
	v_fma_f32 v110, v67, v114, v69
	v_fma_f32 v111, v67, v115, v69
	v_max_f32_e32 v110, 0, v110
	v_max_f32_e32 v111, 0, v111
	v_cvt_pk_bf16_f32 v107, v110, v111
	v_fma_f32 v110, v67, v116, v69
	v_fma_f32 v111, v67, v117, v69
	v_max_f32_e32 v110, 0, v110
	v_max_f32_e32 v111, 0, v111
	v_cvt_pk_bf16_f32 v108, v110, v111
	v_fma_f32 v110, v67, v118, v69
	v_fma_f32 v111, v67, v119, v69
	v_max_f32_e32 v110, 0, v110
	v_max_f32_e32 v111, 0, v111
	v_cvt_pk_bf16_f32 v109, v110, v111
	s_nop 1
	v_mfma_f32_32x32x16_bf16 v[2:17], v[106:109], v[54:57], v[2:17]
	v_fma_f32 v110, v67, v120, v69
	v_fma_f32 v111, v67, v121, v69
	v_max_f32_e32 v110, 0, v110
	v_max_f32_e32 v111, 0, v111
	v_cvt_pk_bf16_f32 v106, v110, v111
	v_fma_f32 v110, v67, v122, v69
	v_fma_f32 v111, v67, v123, v69
	v_max_f32_e32 v110, 0, v110
	v_max_f32_e32 v111, 0, v111
	v_cvt_pk_bf16_f32 v107, v110, v111
	v_fma_f32 v110, v67, v124, v69
	v_fma_f32 v111, v67, v125, v69
	v_max_f32_e32 v110, 0, v110
	v_max_f32_e32 v111, 0, v111
	v_cvt_pk_bf16_f32 v108, v110, v111
	v_fma_f32 v110, v67, v126, v69
	v_fma_f32 v111, v67, v127, v69
	v_max_f32_e32 v110, 0, v110
	v_max_f32_e32 v111, 0, v111
	v_cvt_pk_bf16_f32 v109, v110, v111
	s_nop 1
	v_mfma_f32_32x32x16_bf16 v[2:17], v[106:109], v[58:61], v[2:17]
	v_lshlrev_b32_e32 v39, 1, v34
	ds_read_b128 v[112:115], v39 offset:53248
	ds_read_b128 v[116:119], v39 offset:53760
	ds_read_b128 v[120:123], v39 offset:53504
	s_add_i32 s20, s20, 32
	s_add_i32 s15, s15, -1
	s_cmp_lg_u32 s15, 0
	s_cbranch_scc1 .Lcu_loop
	v_or_b32_e32 v90, s14, v98
	s_branch .LBB8_8
